# grid barrier: XCD leaders no longer add to the per-XCC generation word (nothing polls it since the release-hop edit), which removes one atomic round trip from the last arriver's exit path
# speedup vs baseline: 1.0055x; 1.0055x over previous
; __device__ __forceinline__ unsigned xb_add(unsigned* p, unsigned v) { return __hip_atomic_fetch_add(p, v, __ATOMIC_RELAXED, __HIP_MEMORY_SCOPE_AGENT); }
; __device__ __forceinline__ void xcd_barrier(const XcdBarrier& b) {
;     ...
;             __builtin_amdgcn_fence(__ATOMIC_ACQUIRE, "agent");
;             xb_add(&bar[XB_XGEN(b.x)], 1u);
;             asm volatile("s_waitcnt vmcnt(0)" ::: "memory");
.LBB0_160:
	s_or_b64 exec, exec, s[8:9]
	s_mov_b64 s[8:9], exec
	v_mbcnt_lo_u32_b32 v1, s8, 0
	v_mbcnt_hi_u32_b32 v1, s9, v1
	v_cmp_eq_u32_e32 vcc, 0, v1
	s_waitcnt vmcnt(0)
	buffer_inv sc1
	s_and_saveexec_b64 s[10:11], vcc
	s_cbranch_execz .LBB0_162
	s_bcnt1_i32_b64 s3, s[8:9]
	v_mov_b32_e32 v1, 0x2000
	v_mov_b32_e32 v2, s3
.LBB0_162:
	s_or_b64 exec, exec, s[10:11]
	s_waitcnt vmcnt(0)

; __device__ __forceinline__ unsigned xb_add(unsigned* p, unsigned v) { return __hip_atomic_fetch_add(p, v, __ATOMIC_RELAXED, __HIP_MEMORY_SCOPE_AGENT); }
; __device__ __forceinline__ void xcd_barrier(const XcdBarrier& b) {
;     ...
;             __builtin_amdgcn_fence(__ATOMIC_ACQUIRE, "agent");
;             xb_add(&bar[XB_XGEN(b.x)], 1u);
;             asm volatile("s_waitcnt vmcnt(0)" ::: "memory");
.LBB0_312:
	s_or_b64 exec, exec, s[8:9]
	s_mov_b64 s[8:9], exec
	v_mbcnt_lo_u32_b32 v1, s8, 0
	v_mbcnt_hi_u32_b32 v1, s9, v1
	v_cmp_eq_u32_e32 vcc, 0, v1
	s_waitcnt vmcnt(0)
	buffer_inv sc1
	s_and_saveexec_b64 s[10:11], vcc
	s_cbranch_execz .LBB0_314
	s_bcnt1_i32_b64 s3, s[8:9]
	v_mov_b32_e32 v1, s3
	v_mov_b32_e32 v2, 0x2000
.LBB0_314:
	s_or_b64 exec, exec, s[10:11]
	s_waitcnt vmcnt(0)

; __device__ __forceinline__ unsigned xb_add(unsigned* p, unsigned v) { return __hip_atomic_fetch_add(p, v, __ATOMIC_RELAXED, __HIP_MEMORY_SCOPE_AGENT); }
; __device__ __forceinline__ void xcd_barrier(const XcdBarrier& b) {
;     ...
;             __builtin_amdgcn_fence(__ATOMIC_ACQUIRE, "agent");
;             xb_add(&bar[XB_XGEN(b.x)], 1u);
;             asm volatile("s_waitcnt vmcnt(0)" ::: "memory");
.LBB0_382:
	s_or_b64 exec, exec, s[8:9]
	s_mov_b64 s[8:9], exec
	v_mbcnt_lo_u32_b32 v1, s8, 0
	v_mbcnt_hi_u32_b32 v1, s9, v1
	v_cmp_eq_u32_e32 vcc, 0, v1
	s_waitcnt vmcnt(0)
	buffer_inv sc1
	s_and_saveexec_b64 s[10:11], vcc
	s_cbranch_execz .LBB0_384
	s_bcnt1_i32_b64 s3, s[8:9]
	v_mov_b32_e32 v1, s3
	v_mov_b32_e32 v2, 0x2000
.LBB0_384:
	s_or_b64 exec, exec, s[10:11]
	s_waitcnt vmcnt(0)

; __device__ __forceinline__ unsigned xb_add(unsigned* p, unsigned v) { return __hip_atomic_fetch_add(p, v, __ATOMIC_RELAXED, __HIP_MEMORY_SCOPE_AGENT); }
; __device__ __forceinline__ void xcd_barrier(const XcdBarrier& b) {
;     ...
;             __builtin_amdgcn_fence(__ATOMIC_ACQUIRE, "agent");
;             xb_add(&bar[XB_XGEN(b.x)], 1u);
;             asm volatile("s_waitcnt vmcnt(0)" ::: "memory");
.LBB0_467:
	s_or_b64 exec, exec, s[8:9]
	s_mov_b64 s[8:9], exec
	v_mbcnt_lo_u32_b32 v2, s8, 0
	v_mbcnt_hi_u32_b32 v2, s9, v2
	v_cmp_eq_u32_e32 vcc, 0, v2
	s_waitcnt vmcnt(0)
	buffer_inv sc1
	s_and_saveexec_b64 s[10:11], vcc
	s_cbranch_execz .LBB0_469
	s_bcnt1_i32_b64 s8, s[8:9]
	v_mov_b32_e32 v2, s8
	v_mov_b32_e32 v3, 0x2000
.LBB0_469:
	s_or_b64 exec, exec, s[10:11]
	s_waitcnt vmcnt(0)

; __device__ __forceinline__ unsigned xb_add(unsigned* p, unsigned v) { return __hip_atomic_fetch_add(p, v, __ATOMIC_RELAXED, __HIP_MEMORY_SCOPE_AGENT); }
; __device__ __forceinline__ void xcd_barrier(const XcdBarrier& b) {
;     ...
;             __builtin_amdgcn_fence(__ATOMIC_ACQUIRE, "agent");
;             xb_add(&bar[XB_XGEN(b.x)], 1u);
;             asm volatile("s_waitcnt vmcnt(0)" ::: "memory");
.LBB0_571:
	s_or_b64 exec, exec, s[14:15]
	s_mov_b64 s[14:15], exec
	v_mbcnt_lo_u32_b32 v2, s14, 0
	v_mbcnt_hi_u32_b32 v2, s15, v2
	v_cmp_eq_u32_e32 vcc, 0, v2
	s_waitcnt vmcnt(0)
	buffer_inv sc1
	s_and_saveexec_b64 s[24:25], vcc
	s_cbranch_execz .LBB0_573
	s_bcnt1_i32_b64 s14, s[14:15]
	v_mov_b32_e32 v2, s14
	v_mov_b32_e32 v3, 0x2000
.LBB0_573:
	s_or_b64 exec, exec, s[24:25]
	s_waitcnt vmcnt(0)

; __device__ __forceinline__ unsigned xb_add(unsigned* p, unsigned v) { return __hip_atomic_fetch_add(p, v, __ATOMIC_RELAXED, __HIP_MEMORY_SCOPE_AGENT); }
; __device__ __forceinline__ void xcd_barrier(const XcdBarrier& b) {
;     ...
;             __builtin_amdgcn_fence(__ATOMIC_ACQUIRE, "agent");
;             xb_add(&bar[XB_XGEN(b.x)], 1u);
;             asm volatile("s_waitcnt vmcnt(0)" ::: "memory");
.LBB0_634:
	s_or_b64 exec, exec, s[14:15]
	s_mov_b64 s[14:15], exec
	v_mbcnt_lo_u32_b32 v2, s14, 0
	v_mbcnt_hi_u32_b32 v2, s15, v2
	v_cmp_eq_u32_e32 vcc, 0, v2
	s_waitcnt vmcnt(0)
	buffer_inv sc1
	s_and_saveexec_b64 s[24:25], vcc
	s_cbranch_execz .LBB0_636
	s_bcnt1_i32_b64 s14, s[14:15]
	v_mov_b32_e32 v2, s14
	v_mov_b32_e32 v3, 0x2000
.LBB0_636:
	s_or_b64 exec, exec, s[24:25]
	s_waitcnt vmcnt(0)

; __device__ __forceinline__ unsigned xb_add(unsigned* p, unsigned v) { return __hip_atomic_fetch_add(p, v, __ATOMIC_RELAXED, __HIP_MEMORY_SCOPE_AGENT); }
; __device__ __forceinline__ void xcd_barrier(const XcdBarrier& b) {
;     ...
;             __builtin_amdgcn_fence(__ATOMIC_ACQUIRE, "agent");
;             xb_add(&bar[XB_XGEN(b.x)], 1u);
;             asm volatile("s_waitcnt vmcnt(0)" ::: "memory");
.LBB0_720:
	s_or_b64 exec, exec, s[8:9]
	s_mov_b64 s[8:9], exec
	v_mbcnt_lo_u32_b32 v2, s8, 0
	v_mbcnt_hi_u32_b32 v2, s9, v2
	v_cmp_eq_u32_e32 vcc, 0, v2
	s_waitcnt vmcnt(0)
	buffer_inv sc1
	s_and_saveexec_b64 s[10:11], vcc
	s_cbranch_execz .LBB0_722
	s_bcnt1_i32_b64 s8, s[8:9]
	v_mov_b32_e32 v2, s8
	v_mov_b32_e32 v3, 0x2000
.LBB0_722:
	s_or_b64 exec, exec, s[10:11]
	s_waitcnt vmcnt(0)

; __device__ __forceinline__ unsigned xb_add(unsigned* p, unsigned v) { return __hip_atomic_fetch_add(p, v, __ATOMIC_RELAXED, __HIP_MEMORY_SCOPE_AGENT); }
; __device__ __forceinline__ void xcd_barrier(const XcdBarrier& b) {
;     ...
;             __builtin_amdgcn_fence(__ATOMIC_ACQUIRE, "agent");
;             xb_add(&bar[XB_XGEN(b.x)], 1u);
;             asm volatile("s_waitcnt vmcnt(0)" ::: "memory");
.LBB0_805:
	s_or_b64 exec, exec, s[8:9]
	s_mov_b64 s[8:9], exec
	v_mbcnt_lo_u32_b32 v1, s8, 0
	v_mbcnt_hi_u32_b32 v1, s9, v1
	v_cmp_eq_u32_e32 vcc, 0, v1
	s_waitcnt vmcnt(0)
	buffer_inv sc1
	s_and_saveexec_b64 s[14:15], vcc
	s_cbranch_execz .LBB0_807
	s_bcnt1_i32_b64 s3, s[8:9]
	v_mov_b32_e32 v1, s3
	v_mov_b32_e32 v2, 0x2000
.LBB0_807:
	s_or_b64 exec, exec, s[14:15]
	s_waitcnt vmcnt(0)

; __device__ __forceinline__ unsigned xb_add(unsigned* p, unsigned v) { return __hip_atomic_fetch_add(p, v, __ATOMIC_RELAXED, __HIP_MEMORY_SCOPE_AGENT); }
; __device__ __forceinline__ void xcd_barrier(const XcdBarrier& b) {
;     ...
;             __builtin_amdgcn_fence(__ATOMIC_ACQUIRE, "agent");
;             xb_add(&bar[XB_XGEN(b.x)], 1u);
;             asm volatile("s_waitcnt vmcnt(0)" ::: "memory");
.LBB0_932:
	s_or_b64 exec, exec, s[8:9]
	s_mov_b64 s[8:9], exec
	v_mbcnt_lo_u32_b32 v1, s8, 0
	v_mbcnt_hi_u32_b32 v1, s9, v1
	v_cmp_eq_u32_e32 vcc, 0, v1
	s_waitcnt vmcnt(0)
	buffer_inv sc1
	s_and_saveexec_b64 s[14:15], vcc
	s_cbranch_execz .LBB0_934
	s_bcnt1_i32_b64 s3, s[8:9]
	v_mov_b32_e32 v1, s3
	v_mov_b32_e32 v2, 0x2000
.LBB0_934:
	s_or_b64 exec, exec, s[14:15]
	s_waitcnt vmcnt(0)

; __device__ __forceinline__ unsigned xb_add(unsigned* p, unsigned v) { return __hip_atomic_fetch_add(p, v, __ATOMIC_RELAXED, __HIP_MEMORY_SCOPE_AGENT); }
; __device__ __forceinline__ void xcd_barrier(const XcdBarrier& b) {
;     ...
;             __builtin_amdgcn_fence(__ATOMIC_ACQUIRE, "agent");
;             xb_add(&bar[XB_XGEN(b.x)], 1u);
;             asm volatile("s_waitcnt vmcnt(0)" ::: "memory");
.LBB0_1049:
	s_or_b64 exec, exec, s[8:9]
	s_mov_b64 s[8:9], exec
	v_mbcnt_lo_u32_b32 v1, s8, 0
	v_mbcnt_hi_u32_b32 v1, s9, v1
	v_cmp_eq_u32_e32 vcc, 0, v1
	s_waitcnt vmcnt(0)
	buffer_inv sc1
	s_and_saveexec_b64 s[10:11], vcc
	s_cbranch_execz .LBB0_1051
	s_bcnt1_i32_b64 s3, s[8:9]
	v_mov_b32_e32 v1, s3
	v_mov_b32_e32 v2, 0x2000
.LBB0_1051:
	s_or_b64 exec, exec, s[10:11]
	s_waitcnt vmcnt(0)

; __device__ __forceinline__ unsigned xb_add(unsigned* p, unsigned v) { return __hip_atomic_fetch_add(p, v, __ATOMIC_RELAXED, __HIP_MEMORY_SCOPE_AGENT); }
; __device__ __forceinline__ void xcd_barrier(const XcdBarrier& b) {
;     ...
;             __builtin_amdgcn_fence(__ATOMIC_ACQUIRE, "agent");
;             xb_add(&bar[XB_XGEN(b.x)], 1u);
;             asm volatile("s_waitcnt vmcnt(0)" ::: "memory");
.LBB0_1110:
	s_or_b64 exec, exec, s[8:9]
	s_mov_b64 s[8:9], exec
	v_mbcnt_lo_u32_b32 v2, s8, 0
	v_mbcnt_hi_u32_b32 v2, s9, v2
	v_cmp_eq_u32_e32 vcc, 0, v2
	s_waitcnt vmcnt(0)
	buffer_inv sc1
	s_and_saveexec_b64 s[10:11], vcc
	s_cbranch_execz .LBB0_1112
	s_bcnt1_i32_b64 s2, s[8:9]
	v_mov_b32_e32 v2, s2
	v_mov_b32_e32 v3, 0x2000
.LBB0_1112:
	s_or_b64 exec, exec, s[10:11]
	s_waitcnt vmcnt(0)

; __device__ __forceinline__ unsigned xb_add(unsigned* p, unsigned v) { return __hip_atomic_fetch_add(p, v, __ATOMIC_RELAXED, __HIP_MEMORY_SCOPE_AGENT); }
; __device__ __forceinline__ void xcd_barrier(const XcdBarrier& b) {
;     ...
;             __builtin_amdgcn_fence(__ATOMIC_ACQUIRE, "agent");
;             xb_add(&bar[XB_XGEN(b.x)], 1u);
;             asm volatile("s_waitcnt vmcnt(0)" ::: "memory");
.LBB0_1183:
	s_or_b64 exec, exec, s[8:9]
	s_mov_b64 s[8:9], exec
	v_mbcnt_lo_u32_b32 v2, s8, 0
	v_mbcnt_hi_u32_b32 v2, s9, v2
	v_cmp_eq_u32_e32 vcc, 0, v2
	s_waitcnt vmcnt(0)
	buffer_inv sc1
	s_and_saveexec_b64 s[10:11], vcc
	s_cbranch_execz .LBB0_1185
	s_bcnt1_i32_b64 s2, s[8:9]
	v_mov_b32_e32 v2, s2
	v_mov_b32_e32 v3, 0x2000
.LBB0_1185:
	s_or_b64 exec, exec, s[10:11]
	s_waitcnt vmcnt(0)

; __device__ __forceinline__ unsigned xb_add(unsigned* p, unsigned v) { return __hip_atomic_fetch_add(p, v, __ATOMIC_RELAXED, __HIP_MEMORY_SCOPE_AGENT); }
; __device__ __forceinline__ void xcd_barrier(const XcdBarrier& b) {
;     ...
;             __builtin_amdgcn_fence(__ATOMIC_ACQUIRE, "agent");
;             xb_add(&bar[XB_XGEN(b.x)], 1u);
;             asm volatile("s_waitcnt vmcnt(0)" ::: "memory");
.LBB0_1263:
	s_or_b64 exec, exec, s[8:9]
	s_mov_b64 s[8:9], exec
	v_mbcnt_lo_u32_b32 v2, s8, 0
	v_mbcnt_hi_u32_b32 v2, s9, v2
	v_cmp_eq_u32_e32 vcc, 0, v2
	s_waitcnt vmcnt(0)
	buffer_inv sc1
	s_and_saveexec_b64 s[10:11], vcc
	s_cbranch_execz .LBB0_1265
	s_bcnt1_i32_b64 s2, s[8:9]
	v_mov_b32_e32 v2, s2
	v_mov_b32_e32 v3, 0x2000
.LBB0_1265:
	s_or_b64 exec, exec, s[10:11]
	s_waitcnt vmcnt(0)

; __device__ __forceinline__ unsigned xb_add(unsigned* p, unsigned v) { return __hip_atomic_fetch_add(p, v, __ATOMIC_RELAXED, __HIP_MEMORY_SCOPE_AGENT); }
; __device__ __forceinline__ void xcd_barrier(const XcdBarrier& b) {
;     ...
;             __builtin_amdgcn_fence(__ATOMIC_ACQUIRE, "agent");
;             xb_add(&bar[XB_XGEN(b.x)], 1u);
;             asm volatile("s_waitcnt vmcnt(0)" ::: "memory");
.LBB0_1380:
	s_or_b64 exec, exec, s[8:9]
	s_mov_b64 s[8:9], exec
	v_mbcnt_lo_u32_b32 v1, s8, 0
	v_mbcnt_hi_u32_b32 v1, s9, v1
	v_cmp_eq_u32_e32 vcc, 0, v1
	s_waitcnt vmcnt(0)
	buffer_inv sc1
	s_and_saveexec_b64 s[10:11], vcc
	s_cbranch_execz .LBB0_1382
	s_bcnt1_i32_b64 s3, s[8:9]
	v_mov_b32_e32 v1, s3
	v_mov_b32_e32 v2, 0x2000
.LBB0_1382:
	s_or_b64 exec, exec, s[10:11]
	s_waitcnt vmcnt(0)

; __device__ __forceinline__ unsigned xb_add(unsigned* p, unsigned v) { return __hip_atomic_fetch_add(p, v, __ATOMIC_RELAXED, __HIP_MEMORY_SCOPE_AGENT); }
; __device__ __forceinline__ void xcd_barrier(const XcdBarrier& b) {
;     ...
;             __builtin_amdgcn_fence(__ATOMIC_ACQUIRE, "agent");
;             xb_add(&bar[XB_XGEN(b.x)], 1u);
;             asm volatile("s_waitcnt vmcnt(0)" ::: "memory");
.LBB0_1458:
	s_or_b64 exec, exec, s[8:9]
	s_mov_b64 s[8:9], exec
	v_mbcnt_lo_u32_b32 v1, s8, 0
	v_mbcnt_hi_u32_b32 v1, s9, v1
	v_cmp_eq_u32_e32 vcc, 0, v1
	s_waitcnt vmcnt(0)
	buffer_inv sc1
	s_and_saveexec_b64 s[10:11], vcc
	s_cbranch_execz .LBB0_1460
	s_bcnt1_i32_b64 s8, s[8:9]
	v_mov_b32_e32 v1, s8
	v_mov_b32_e32 v2, 0x2000
.LBB0_1460:
	s_or_b64 exec, exec, s[10:11]
	s_waitcnt vmcnt(0)

; __device__ __forceinline__ unsigned xb_add(unsigned* p, unsigned v) { return __hip_atomic_fetch_add(p, v, __ATOMIC_RELAXED, __HIP_MEMORY_SCOPE_AGENT); }
; __device__ __forceinline__ void xcd_barrier(const XcdBarrier& b) {
;     ...
;             __builtin_amdgcn_fence(__ATOMIC_ACQUIRE, "agent");
;             xb_add(&bar[XB_XGEN(b.x)], 1u);
;             asm volatile("s_waitcnt vmcnt(0)" ::: "memory");
.LBB0_1535:
	s_bcnt1_i32_b64 s3, s[8:9]
	v_mov_b32_e32 v1, s3
	v_mov_b32_e32 v2, 0x2000
	s_getpc_b64 s[98:99]
